# v39 + per-barrier L1 invalidate issued asynchronously by wave 0 at the START of each phase (off the barrier arrival path; no cross-workgroup read-after-write exists inside a phase)
# baseline (speedup 1.0000x reference)
.LBB0_127:
	s_cmp_lg_u32 s88, 0
	s_cbranch_scc1 .Linvp_0
	buffer_inv sc1
